# speedup vs baseline: 1.0477x; 1.0212x over previous
_Z16sum_layer_kernelPKfS0_Pf:
	s_load_dwordx4 s[4:7], s[0:1], 0x0
	s_load_dwordx2 s[8:9], s[0:1], 0x10
	v_and_b32_e32 v40, 31, v0
	v_bfe_u32 v41, v0, 5, 1
	v_lshrrev_b32_e32 v42, 6, v0
	v_and_b32_e32 v43, 7, v0
	v_bfe_u32 v44, v0, 3, 3
	v_and_b32_e32 v45, 63, v0
	s_lshl_b32 s3, s2, 12
	s_lshl_b32 s19, s2, 7
	v_lshlrev_b32_e32 v1, 11, v41
	v_lshl_or_b32 v1, v40, 2, v1
	v_lshlrev_b32_e32 v46, 4, v43
	v_lshl_add_u32 v35, v44, 16, v46
	v_lshl_add_u32 v35, v42, 21, v35
	v_add_u32_e32 v35, s19, v35
	v_lshlrev_b32_e32 v36, 2, v40
	v_lshl_add_u32 v36, v41, 18, v36
	v_lshl_add_u32 v36, v42, 21, v36
	v_add_u32_e32 v36, s19, v36
	v_mul_u32_u24_e32 v37, 0x1200, v42
	v_mul_u32_u24_e32 v38, 0x90, v44
	v_add3_u32 v38, v37, v38, v46
	v_mul_u32_u24_e32 v39, 0x90, v40
	v_lshlrev_b32_e32 v47, 6, v41
	v_add3_u32 v39, v37, v39, v47
	v_cmp_gt_u32_e32 vcc, 32, v45
	v_mov_b32_e32 v48, 0xc1600000
	s_mov_b32 s16, 0x3fb8aa3b
	s_mov_b32 s17, 0x3f317218
	s_mov_b32 s20, 0x80000
	s_mov_b32 s21, 0x100000
	s_mov_b32 s22, 0x180000
	s_lshl_b32 s24, 1, 16
	s_lshl_b32 s25, 2, 16
	s_lshl_b32 s26, 3, 16
	s_lshl_b32 s27, 8, 16
	s_lshl_b32 s28, 9, 16
	s_lshl_b32 s29, 10, 16
	s_lshl_b32 s30, 11, 16
	s_lshl_b32 s31, 16, 16
	s_lshl_b32 s32, 17, 16
	s_lshl_b32 s33, 18, 16
	s_lshl_b32 s34, 19, 16
	s_lshl_b32 s35, 24, 16
	s_lshl_b32 s36, 25, 16
	s_lshl_b32 s37, 26, 16
	s_lshl_b32 s38, 27, 16
	s_mov_b32 s14, 0x200000
	s_mov_b32 s15, 0x20000
	s_waitcnt lgkmcnt(0)
	s_mov_b32 s12, s6
	s_and_b32 s13, s7, 0xffff
	s_and_b32 s5, s5, 0xffff
	s_mov_b32 s6, 0x800000
	s_mov_b32 s7, s15
	s_and_b32 s9, s9, 0xffff
	s_mov_b32 s10, s6
	s_mov_b32 s11, s15
	buffer_load_dword v18, v1, s[12:15], s3 offen nt
	buffer_load_dword v19, v1, s[12:15], s3 offen offset:128 nt
	buffer_load_dword v20, v1, s[12:15], s3 offen offset:256 nt
	buffer_load_dword v21, v1, s[12:15], s3 offen offset:384 nt
	buffer_load_dword v22, v1, s[12:15], s3 offen offset:512 nt
	buffer_load_dword v23, v1, s[12:15], s3 offen offset:640 nt
	buffer_load_dword v24, v1, s[12:15], s3 offen offset:768 nt
	buffer_load_dword v25, v1, s[12:15], s3 offen offset:896 nt
	buffer_load_dword v26, v1, s[12:15], s3 offen offset:1024 nt
	buffer_load_dword v27, v1, s[12:15], s3 offen offset:1152 nt
	buffer_load_dword v28, v1, s[12:15], s3 offen offset:1280 nt
	buffer_load_dword v29, v1, s[12:15], s3 offen offset:1408 nt
	buffer_load_dword v30, v1, s[12:15], s3 offen offset:1536 nt
	buffer_load_dword v31, v1, s[12:15], s3 offen offset:1664 nt
	buffer_load_dword v32, v1, s[12:15], s3 offen offset:1792 nt
	buffer_load_dword v33, v1, s[12:15], s3 offen offset:1920 nt
	buffer_load_dwordx4 v[2:5], v35, s[4:7], 0 offen nt
	buffer_load_dwordx4 v[6:9], v35, s[4:7], s20 offen nt
	buffer_load_dwordx4 v[10:13], v35, s[4:7], s21 offen nt
	buffer_load_dwordx4 v[14:17], v35, s[4:7], s22 offen nt
	s_waitcnt vmcnt(4)
	v_max3_f32 v49, v18, v19, v20
	v_max3_f32 v50, v21, v22, v23
	v_max3_f32 v49, v49, v24, v25
	v_max3_f32 v50, v50, v26, v27
	v_max3_f32 v49, v49, v28, v29
	v_max3_f32 v50, v50, v30, v31
	v_max3_f32 v49, v49, v32, v33
	v_max_f32_e32 v49, v49, v50
	v_mov_b32_e32 v50, v49
	s_nop 1
	v_permlane32_swap_b32_e32 v49, v50
	v_max_f32_e32 v49, v49, v50
	v_fmamk_f32 v49, v49, 0x3fb8aa3b, v48
	v_fma_f32 v18, v18, s16, -v49
	v_exp_f32_e32 v18, v18
	v_fma_f32 v19, v19, s16, -v49
	v_exp_f32_e32 v19, v19
	v_fma_f32 v20, v20, s16, -v49
	v_exp_f32_e32 v20, v20
	v_fma_f32 v21, v21, s16, -v49
	v_exp_f32_e32 v21, v21
	v_fma_f32 v22, v22, s16, -v49
	v_exp_f32_e32 v22, v22
	v_fma_f32 v23, v23, s16, -v49
	v_exp_f32_e32 v23, v23
	v_fma_f32 v24, v24, s16, -v49
	v_exp_f32_e32 v24, v24
	v_fma_f32 v25, v25, s16, -v49
	v_exp_f32_e32 v25, v25
	v_fma_f32 v26, v26, s16, -v49
	v_exp_f32_e32 v26, v26
	v_fma_f32 v27, v27, s16, -v49
	v_exp_f32_e32 v27, v27
	v_fma_f32 v28, v28, s16, -v49
	v_exp_f32_e32 v28, v28
	v_fma_f32 v29, v29, s16, -v49
	v_exp_f32_e32 v29, v29
	v_fma_f32 v30, v30, s16, -v49
	v_exp_f32_e32 v30, v30
	v_fma_f32 v31, v31, s16, -v49
	v_exp_f32_e32 v31, v31
	v_fma_f32 v32, v32, s16, -v49
	v_exp_f32_e32 v32, v32
	v_fma_f32 v33, v33, s16, -v49
	v_exp_f32_e32 v33, v33
	v_add_f32_e32 v50, v18, v19
	v_add_f32_e32 v51, v20, v21
	v_add_f32_e32 v50, v50, v22
	v_add_f32_e32 v51, v51, v23
	v_add_f32_e32 v50, v50, v24
	v_add_f32_e32 v51, v51, v25
	v_add_f32_e32 v50, v50, v26
	v_add_f32_e32 v51, v51, v27
	v_add_f32_e32 v50, v50, v28
	v_add_f32_e32 v51, v51, v29
	v_add_f32_e32 v50, v50, v30
	v_add_f32_e32 v51, v51, v31
	v_add_f32_e32 v50, v50, v32
	v_add_f32_e32 v51, v51, v33
	v_add_f32_e32 v50, v50, v51
	v_mov_b32_e32 v51, v50
	s_nop 1
	v_permlane32_swap_b32_e32 v50, v51
	v_add_f32_e32 v50, v50, v51
	v_log_f32_e32 v50, v50
	v_cvt_pk_f16_f32 v52, v18, v19
	v_cvt_pk_f16_f32 v53, v20, v21
	v_cvt_pk_f16_f32 v54, v22, v23
	v_cvt_pk_f16_f32 v55, v24, v25
	v_cvt_pk_f16_f32 v56, v26, v27
	v_cvt_pk_f16_f32 v57, v28, v29
	v_cvt_pk_f16_f32 v58, v30, v31
	v_cvt_pk_f16_f32 v59, v32, v33
	v_add_f32_e32 v50, 0x41600000, v50
	v_mul_f32_e32 v50, 0xbf317218, v50
	v_cndmask_b32_e64 v51, v50, 1.0, vcc
	s_waitcnt vmcnt(3)
	ds_write_b128 v38, v[2:5]
	s_waitcnt vmcnt(2)
	ds_write_b128 v38, v[6:9] offset:1152
	s_waitcnt vmcnt(1)
	ds_write_b128 v38, v[10:13] offset:2304
	s_waitcnt vmcnt(0)
	ds_write_b128 v38, v[14:17] offset:3456
	ds_read_b128 v[60:63], v39
	ds_read_b128 v[64:67], v39 offset:16
	ds_read_b128 v[68:71], v39 offset:32
	ds_read_b128 v[72:75], v39 offset:48
	s_waitcnt lgkmcnt(2)
	v_max3_f32 v76, v60, v61, v62
	v_max3_f32 v77, v63, v64, v65
	v_max_f32_e32 v76, v76, v66
	v_max_f32_e32 v77, v77, v67
	s_waitcnt lgkmcnt(0)
	v_max3_f32 v76, v76, v68, v69
	v_max3_f32 v77, v77, v70, v71
	v_max3_f32 v76, v76, v72, v73
	v_max3_f32 v77, v77, v74, v75
	v_max_f32_e32 v76, v76, v77
	v_mov_b32_e32 v77, v76
	s_nop 1
	v_permlane32_swap_b32_e32 v76, v77
	v_max_f32_e32 v76, v76, v77
	v_cndmask_b32_e32 v78, 1.0, v76, vcc
	v_fmamk_f32 v79, v76, 0x3fb8aa3b, v48
	v_fma_f32 v60, v60, s16, -v79
	v_mfma_f32_32x32x2_f32 v[80:95], v78, v51, 0
	v_exp_f32_e32 v60, v60
	v_fma_f32 v61, v61, s16, -v79
	v_exp_f32_e32 v61, v61
	v_fma_f32 v62, v62, s16, -v79
	v_exp_f32_e32 v62, v62
	v_fma_f32 v63, v63, s16, -v79
	v_exp_f32_e32 v63, v63
	v_fma_f32 v64, v64, s16, -v79
	v_exp_f32_e32 v64, v64
	v_fma_f32 v65, v65, s16, -v79
	v_exp_f32_e32 v65, v65
	v_fma_f32 v66, v66, s16, -v79
	v_exp_f32_e32 v66, v66
	v_fma_f32 v67, v67, s16, -v79
	v_exp_f32_e32 v67, v67
	v_fma_f32 v68, v68, s16, -v79
	v_exp_f32_e32 v68, v68
	v_cvt_pk_f16_f32 v96, v60, v61
	v_cvt_pk_f16_f32 v97, v62, v63
	v_cvt_pk_f16_f32 v98, v64, v65
	v_cvt_pk_f16_f32 v99, v66, v67
	v_fma_f32 v69, v69, s16, -v79
	v_exp_f32_e32 v69, v69
	v_fma_f32 v70, v70, s16, -v79
	v_exp_f32_e32 v70, v70
	v_mfma_f32_32x32x16_f16 v[104:119], v[96:99], v[52:55], 0
	v_fma_f32 v71, v71, s16, -v79
	v_exp_f32_e32 v71, v71
	v_fma_f32 v72, v72, s16, -v79
	v_exp_f32_e32 v72, v72
	v_fma_f32 v73, v73, s16, -v79
	v_exp_f32_e32 v73, v73
	v_fma_f32 v74, v74, s16, -v79
	v_exp_f32_e32 v74, v74
	v_fma_f32 v75, v75, s16, -v79
	v_exp_f32_e32 v75, v75
	v_cvt_pk_f16_f32 v100, v68, v69
	v_cvt_pk_f16_f32 v101, v70, v71
	v_cvt_pk_f16_f32 v102, v72, v73
	v_cvt_pk_f16_f32 v103, v74, v75
	s_nop 1
	v_mfma_f32_32x32x16_f16 v[104:119], v[100:103], v[56:59], v[104:119]
	s_nop 11
	v_log_f32_e32 v104, v104
	v_log_f32_e32 v105, v105
	v_log_f32_e32 v106, v106
	v_fmac_f32_e32 v80, s17, v104
	buffer_store_dword v80, v36, s[8:11], 0 offen
	v_log_f32_e32 v107, v107
	v_fmac_f32_e32 v81, s17, v105
	buffer_store_dword v81, v36, s[8:11], s24 offen
	v_log_f32_e32 v108, v108
	v_fmac_f32_e32 v82, s17, v106
	buffer_store_dword v82, v36, s[8:11], s25 offen
	v_log_f32_e32 v109, v109
	v_fmac_f32_e32 v83, s17, v107
	buffer_store_dword v83, v36, s[8:11], s26 offen
	v_log_f32_e32 v110, v110
	v_fmac_f32_e32 v84, s17, v108
	buffer_store_dword v84, v36, s[8:11], s27 offen
	v_log_f32_e32 v111, v111
	v_fmac_f32_e32 v85, s17, v109
	buffer_store_dword v85, v36, s[8:11], s28 offen
	v_log_f32_e32 v112, v112
	v_fmac_f32_e32 v86, s17, v110
	buffer_store_dword v86, v36, s[8:11], s29 offen
	v_log_f32_e32 v113, v113
	v_fmac_f32_e32 v87, s17, v111
	buffer_store_dword v87, v36, s[8:11], s30 offen
	v_log_f32_e32 v114, v114
	v_fmac_f32_e32 v88, s17, v112
	buffer_store_dword v88, v36, s[8:11], s31 offen
	v_log_f32_e32 v115, v115
	v_fmac_f32_e32 v89, s17, v113
	buffer_store_dword v89, v36, s[8:11], s32 offen
	v_log_f32_e32 v116, v116
	v_fmac_f32_e32 v90, s17, v114
	buffer_store_dword v90, v36, s[8:11], s33 offen
	v_log_f32_e32 v117, v117
	v_fmac_f32_e32 v91, s17, v115
	buffer_store_dword v91, v36, s[8:11], s34 offen
	v_log_f32_e32 v118, v118
	v_fmac_f32_e32 v92, s17, v116
	buffer_store_dword v92, v36, s[8:11], s35 offen
	v_log_f32_e32 v119, v119
	v_fmac_f32_e32 v93, s17, v117
	buffer_store_dword v93, v36, s[8:11], s36 offen
	v_fmac_f32_e32 v94, s17, v118
	buffer_store_dword v94, v36, s[8:11], s37 offen
	v_fmac_f32_e32 v95, s17, v119
	buffer_store_dword v95, v36, s[8:11], s38 offen
	s_endpgm

	.amdhsa_kernel _Z16sum_layer_kernelPKfS0_Pf
		.amdhsa_group_segment_fixed_size 18432
		.amdhsa_private_segment_fixed_size 0
		.amdhsa_kernarg_size 24
		.amdhsa_user_sgpr_count 2
		.amdhsa_user_sgpr_dispatch_ptr 0
		.amdhsa_user_sgpr_queue_ptr 0
		.amdhsa_user_sgpr_kernarg_segment_ptr 1
		.amdhsa_user_sgpr_dispatch_id 0
		.amdhsa_user_sgpr_kernarg_preload_length 0
		.amdhsa_user_sgpr_kernarg_preload_offset 0
		.amdhsa_user_sgpr_private_segment_size 0
		.amdhsa_uses_dynamic_stack 0
		.amdhsa_enable_private_segment 0
		.amdhsa_system_sgpr_workgroup_id_x 1
		.amdhsa_system_sgpr_workgroup_id_y 0
		.amdhsa_system_sgpr_workgroup_id_z 0
		.amdhsa_system_sgpr_workgroup_info 0
		.amdhsa_system_vgpr_workitem_id 0
		.amdhsa_next_free_vgpr 120
		.amdhsa_next_free_sgpr 39
		.amdhsa_accum_offset 120
		.amdhsa_reserve_vcc 1
		.amdhsa_float_round_mode_32 0
		.amdhsa_float_round_mode_16_64 0
		.amdhsa_float_denorm_mode_32 3
		.amdhsa_float_denorm_mode_16_64 3
		.amdhsa_dx10_clamp 1
		.amdhsa_ieee_mode 1
		.amdhsa_fp16_overflow 0
		.amdhsa_tg_split 0
		.amdhsa_exception_fp_ieee_invalid_op 0
		.amdhsa_exception_fp_denorm_src 0
		.amdhsa_exception_fp_ieee_div_zero 0
		.amdhsa_exception_fp_ieee_overflow 0
		.amdhsa_exception_fp_ieee_underflow 0
		.amdhsa_exception_fp_ieee_inexact 0
		.amdhsa_exception_int_div_zero 0
	.end_amdhsa_kernel

amdhsa.kernels:
  - .agpr_count:     0
    .args:
      - .address_space:  global
        .offset:         0
        .size:           8
        .value_kind:     global_buffer
      - .address_space:  global
        .offset:         8
        .size:           8
        .value_kind:     global_buffer
      - .address_space:  global
        .offset:         16
        .size:           8
        .value_kind:     global_buffer
    .group_segment_fixed_size: 18432
    .kernarg_segment_align: 8
    .kernarg_segment_size: 24
    .language:       OpenCL C
    .language_version:
      - 2
      - 0
    .max_flat_workgroup_size: 256
    .name:           _Z16sum_layer_kernelPKfS0_Pf
    .private_segment_fixed_size: 0
    .sgpr_count:     45
    .sgpr_spill_count: 0
    .symbol:         _Z16sum_layer_kernelPKfS0_Pf.kd
    .uniform_work_group_size: 1
    .uses_dynamic_stack: false
    .vgpr_count:     120
    .vgpr_spill_count: 0
    .wavefront_size: 64
